# speedup vs baseline: 1.0376x; 1.0075x over previous
_Z11center_mainPKfPKcS0_Pf:
	s_load_dwordx4 s[4:7], s[0:1], 0x0
	s_load_dwordx4 s[8:11], s[0:1], 0x10
	s_and_b32 s3, s2, 7
	s_lshr_b32 s12, s2, 3
	s_mov_b32 s30, s2
	v_lshrrev_b32_e32 v1, 6, v0
	v_and_b32_e32 v2, 63, v0
	v_bfe_u32 v3, v0, 3, 3
	v_and_b32_e32 v4, 7, v0
	v_lshrrev_b32_e32 v5, 7, v0
	v_bfe_u32 v6, v0, 6, 1
	v_lshl_or_b32 v7, v5, 3, v3
	v_lshlrev_b32_e32 v8, 10, v7
	v_lshl_or_b32 v8, v6, 9, v8
	v_lshl_or_b32 v226, v4, 4, v8
	v_lshlrev_b32_e32 v17, 15, v1
	v_lshl_or_b32 v227, v2, 5, v17
	v_lshlrev_b32_e32 v237, 3, v0
	s_lshl_b32 s13, s3, 22
	s_lshl_b32 s14, s12, 15
	s_add_u32 s13, s13, s14
	s_lshl_b32 s15, s3, 18
	s_lshl_b32 s28, s3, 12
	s_waitcnt lgkmcnt(0)
	s_add_u32 s16, s4, s13
	s_addc_u32 s17, s5, 0
	global_load_dwordx4 v[194:197], v226, s[16:17] offset:0 nt
	global_load_dwordx4 v[198:201], v226, s[16:17] offset:128 nt
	global_load_dwordx4 v[202:205], v226, s[16:17] offset:256 nt
	global_load_dwordx4 v[206:209], v226, s[16:17] offset:384 nt
	s_add_u32 s8, s8, s28
	s_addc_u32 s9, s9, 0
	global_load_dwordx2 v[238:239], v237, s[8:9]
	s_add_u32 s24, s6, s15
	s_addc_u32 s25, s7, 0
	s_add_u32 s32, s24, 0x1000
	s_addc_u32 s33, s25, 0
	s_add_u32 s34, s24, 0x2000
	s_addc_u32 s35, s25, 0
	s_add_u32 s36, s24, 0x3000
	s_addc_u32 s37, s25, 0
	s_add_u32 s38, s24, 0x4000
	s_addc_u32 s39, s25, 0
	s_add_u32 s40, s24, 0x5000
	s_addc_u32 s41, s25, 0
	s_add_u32 s42, s24, 0x6000
	s_addc_u32 s43, s25, 0
	s_add_u32 s44, s24, 0x7000
	s_addc_u32 s45, s25, 0
	global_load_dwordx4 v[34:37], v227, s[24:25] offset:0
	global_load_dwordx4 v[38:41], v227, s[24:25] offset:16
	global_load_dwordx4 v[26:29], v227, s[24:25] offset:2048
	global_load_dwordx4 v[30:33], v227, s[24:25] offset:2064
	global_load_dwordx4 v[50:53], v227, s[32:33] offset:0
	global_load_dwordx4 v[54:57], v227, s[32:33] offset:16
	global_load_dwordx4 v[42:45], v227, s[32:33] offset:2048
	global_load_dwordx4 v[46:49], v227, s[32:33] offset:2064
	global_load_dwordx4 v[18:21], v227, s[34:35] offset:0
	global_load_dwordx4 v[22:25], v227, s[34:35] offset:16
	global_load_dwordx4 v[130:133], v227, s[34:35] offset:2048
	global_load_dwordx4 v[134:137], v227, s[34:35] offset:2064
	global_load_dwordx4 v[122:125], v227, s[36:37] offset:0
	global_load_dwordx4 v[126:129], v227, s[36:37] offset:16
	global_load_dwordx4 v[138:141], v227, s[36:37] offset:2048
	global_load_dwordx4 v[142:145], v227, s[36:37] offset:2064
	global_load_dwordx4 v[98:101], v227, s[38:39] offset:0
	global_load_dwordx4 v[102:105], v227, s[38:39] offset:16
	global_load_dwordx4 v[90:93], v227, s[38:39] offset:2048
	global_load_dwordx4 v[94:97], v227, s[38:39] offset:2064
	global_load_dwordx4 v[114:117], v227, s[40:41] offset:0
	global_load_dwordx4 v[118:121], v227, s[40:41] offset:16
	global_load_dwordx4 v[106:109], v227, s[40:41] offset:2048
	global_load_dwordx4 v[110:113], v227, s[40:41] offset:2064
	global_load_dwordx4 v[58:61], v227, s[42:43] offset:0
	global_load_dwordx4 v[62:65], v227, s[42:43] offset:16
	global_load_dwordx4 v[66:69], v227, s[42:43] offset:2048
	global_load_dwordx4 v[70:73], v227, s[42:43] offset:2064
	global_load_dwordx4 v[74:77], v227, s[44:45] offset:0
	global_load_dwordx4 v[78:81], v227, s[44:45] offset:16
	global_load_dwordx4 v[82:85], v227, s[44:45] offset:2048
	global_load_dwordx4 v[86:89], v227, s[44:45] offset:2064
	s_add_u32 s18, s16, 0x100000
	s_addc_u32 s19, s17, 0
	s_add_u32 s20, s16, 0x200000
	s_addc_u32 s21, s17, 0
	s_add_u32 s22, s16, 0x300000
	s_addc_u32 s23, s17, 0
	v_mul_u32_u24_e32 v9, 0x110, v7
	v_lshl_add_u32 v9, v6, 7, v9
	v_lshl_add_u32 v228, v4, 4, v9
	v_lshlrev_b32_e32 v10, 6, v7
	v_lshl_or_b32 v10, v6, 5, v10
	v_lshl_or_b32 v229, v4, 2, v10
	v_and_b32_e32 v11, 31, v0
	v_bfe_u32 v12, v0, 5, 1
	v_mul_u32_u24_e32 v13, 0x110, v11
	v_lshl_add_u32 v230, v12, 5, v13
	v_lshlrev_b32_e32 v14, 9, v1
	v_lshl_or_b32 v231, v12, 4, v14
	v_xor_b32_e32 v15, 32, v2
	v_lshlrev_b32_e32 v232, 2, v15
	v_xor_b32_e32 v15, 16, v2
	v_lshlrev_b32_e32 v247, 2, v15
	v_lshlrev_b32_e32 v16, 7, v1
	v_lshl_or_b32 v233, v11, 2, v16
	v_mov_b32_e32 v234, 0x7f7f7f7f
	s_waitcnt vmcnt(32)
	ds_write_b64 v237, v[238:239] offset:34816
	v_mul_f32_e32 v244, v194, v194
	v_mul_f32_e32 v245, v198, v198
	v_cvt_pk_fp8_f32 v240, v194, v195
	v_cvt_pk_fp8_f32 v241, v198, v199
	v_cvt_pk_fp8_f32 v242, v202, v203
	v_cvt_pk_fp8_f32 v243, v206, v207
	v_fmac_f32_e32 v244, v195, v195
	v_fmac_f32_e32 v245, v199, v199
	v_fmac_f32_e32 v244, v196, v196
	v_fmac_f32_e32 v245, v200, v200
	v_fmac_f32_e32 v244, v197, v197
	v_fmac_f32_e32 v245, v201, v201
	v_fmac_f32_e32 v244, v202, v202
	v_fmac_f32_e32 v245, v206, v206
	v_fmac_f32_e32 v244, v203, v203
	v_fmac_f32_e32 v245, v207, v207
	v_fmac_f32_e32 v244, v204, v204
	v_fmac_f32_e32 v245, v208, v208
	v_fmac_f32_e32 v244, v205, v205
	v_fmac_f32_e32 v245, v209, v209
	v_cvt_pk_fp8_f32 v240, v196, v197 op_sel:[0,0,1]
	v_cvt_pk_fp8_f32 v241, v200, v201 op_sel:[0,0,1]
	v_cvt_pk_fp8_f32 v242, v204, v205 op_sel:[0,0,1]
	v_cvt_pk_fp8_f32 v243, v208, v209 op_sel:[0,0,1]
	v_add_f32_e32 v244, v244, v245
	s_nop 0
	ds_write_b128 v228, v[240:243] offset:0
	ds_write_b32 v229, v244 offset:38912
	s_waitcnt lgkmcnt(0)
	s_barrier
	ds_read_b128 v[162:165], v230 offset:0
	ds_read_b128 v[166:169], v230 offset:16
	ds_read_b128 v[2:5], v231 offset:34816
	ds_read_b128 v[6:9], v231 offset:34848
	ds_read_b128 v[10:13], v231 offset:34880
	ds_read_b128 v[14:17], v231 offset:34912
	ds_read_b128 v[170:173], v230 offset:64
	ds_read_b128 v[174:177], v230 offset:80
	ds_read_b128 v[178:181], v230 offset:128
	ds_read_b128 v[182:185], v230 offset:144
	ds_read_b128 v[186:189], v230 offset:192
	ds_read_b128 v[190:193], v230 offset:208
	s_waitcnt vmcnt(30) lgkmcnt(6)
	v_mfma_f32_32x32x64_f8f6f4 v[2:17], v[34:41], v[162:169], v[2:17]
	s_waitcnt vmcnt(28) lgkmcnt(4)
	v_mfma_f32_32x32x64_f8f6f4 v[2:17], v[26:33], v[170:177], v[2:17]
	ds_read_b128 v[146:149], v231 offset:34944
	ds_read_b128 v[150:153], v231 offset:34976
	ds_read_b128 v[154:157], v231 offset:35008
	ds_read_b128 v[158:161], v231 offset:35040
	s_waitcnt vmcnt(26) lgkmcnt(6)
	v_mfma_f32_32x32x64_f8f6f4 v[2:17], v[50:57], v[178:185], v[2:17]
	s_waitcnt vmcnt(24) lgkmcnt(4)
	v_mfma_f32_32x32x64_f8f6f4 v[2:17], v[42:49], v[186:193], v[2:17]
	global_load_dwordx4 v[210:213], v226, s[18:19] offset:0 nt
	global_load_dwordx4 v[214:217], v226, s[18:19] offset:128 nt
	global_load_dwordx4 v[218:221], v226, s[18:19] offset:256 nt
	global_load_dwordx4 v[222:225], v226, s[18:19] offset:384 nt
	s_waitcnt lgkmcnt(0)
	s_waitcnt vmcnt(26)
	v_mfma_f32_32x32x64_f8f6f4 v[146:161], v[18:25], v[162:169], v[146:161]
	s_waitcnt vmcnt(24)
	v_mfma_f32_32x32x64_f8f6f4 v[146:161], v[130:137], v[170:177], v[146:161]
	v_min3_f32 v2, v2, v3, v4
	v_min3_f32 v5, v5, v6, v7
	v_min3_f32 v8, v8, v9, v10
	v_min3_f32 v11, v11, v12, v13
	v_min3_f32 v14, v14, v15, v16
	v_min3_f32 v2, v2, v5, v8
	v_min3_f32 v11, v11, v14, v17
	v_min_f32_e32 v235, v2, v11
	ds_read_b128 v[2:5], v231 offset:35072
	ds_read_b128 v[6:9], v231 offset:35104
	ds_read_b128 v[10:13], v231 offset:35136
	ds_read_b128 v[14:17], v231 offset:35168
	s_waitcnt vmcnt(22)
	v_mfma_f32_32x32x64_f8f6f4 v[146:161], v[122:129], v[178:185], v[146:161]
	s_waitcnt vmcnt(20)
	v_mfma_f32_32x32x64_f8f6f4 v[146:161], v[138:145], v[186:193], v[146:161]
	s_waitcnt vmcnt(18) lgkmcnt(0)
	v_mfma_f32_32x32x64_f8f6f4 v[2:17], v[98:105], v[162:169], v[2:17]
	s_waitcnt vmcnt(16)
	v_mfma_f32_32x32x64_f8f6f4 v[2:17], v[90:97], v[170:177], v[2:17]
	v_min3_f32 v146, v146, v147, v148
	v_min3_f32 v149, v149, v150, v151
	v_min3_f32 v152, v152, v153, v154
	v_min3_f32 v155, v155, v156, v157
	v_min3_f32 v158, v158, v159, v160
	v_min3_f32 v146, v146, v149, v152
	v_min3_f32 v155, v155, v158, v161
	v_min3_f32 v235, v235, v146, v155
	ds_read_b128 v[146:149], v231 offset:35200
	ds_read_b128 v[150:153], v231 offset:35232
	ds_read_b128 v[154:157], v231 offset:35264
	ds_read_b128 v[158:161], v231 offset:35296
	s_waitcnt vmcnt(14)
	v_mfma_f32_32x32x64_f8f6f4 v[2:17], v[114:121], v[178:185], v[2:17]
	s_waitcnt vmcnt(12)
	v_mfma_f32_32x32x64_f8f6f4 v[2:17], v[106:113], v[186:193], v[2:17]
	s_waitcnt vmcnt(10) lgkmcnt(0)
	v_mfma_f32_32x32x64_f8f6f4 v[146:161], v[58:65], v[162:169], v[146:161]
	s_waitcnt vmcnt(8)
	v_mfma_f32_32x32x64_f8f6f4 v[146:161], v[66:73], v[170:177], v[146:161]
	v_min3_f32 v2, v2, v3, v4
	v_min3_f32 v5, v5, v6, v7
	v_min3_f32 v8, v8, v9, v10
	v_min3_f32 v11, v11, v12, v13
	v_min3_f32 v14, v14, v15, v16
	v_min3_f32 v2, v2, v5, v8
	v_min3_f32 v11, v11, v14, v17
	v_min3_f32 v235, v235, v2, v11
	ds_read_b128 v[2:5], v231 offset:34816
	ds_read_b128 v[6:9], v231 offset:34848
	ds_read_b128 v[10:13], v231 offset:34880
	ds_read_b128 v[14:17], v231 offset:34912
	s_waitcnt vmcnt(6)
	v_mfma_f32_32x32x64_f8f6f4 v[146:161], v[74:81], v[178:185], v[146:161]
	s_waitcnt vmcnt(4)
	v_mfma_f32_32x32x64_f8f6f4 v[146:161], v[82:89], v[186:193], v[146:161]
	s_waitcnt vmcnt(0)
	v_mul_f32_e32 v244, v210, v210
	v_mul_f32_e32 v245, v214, v214
	v_cvt_pk_fp8_f32 v240, v210, v211
	v_cvt_pk_fp8_f32 v241, v214, v215
	v_cvt_pk_fp8_f32 v242, v218, v219
	v_cvt_pk_fp8_f32 v243, v222, v223
	v_fmac_f32_e32 v244, v211, v211
	v_fmac_f32_e32 v245, v215, v215
	v_fmac_f32_e32 v244, v212, v212
	v_fmac_f32_e32 v245, v216, v216
	v_fmac_f32_e32 v244, v213, v213
	v_fmac_f32_e32 v245, v217, v217
	v_fmac_f32_e32 v244, v218, v218
	v_fmac_f32_e32 v245, v222, v222
	v_fmac_f32_e32 v244, v219, v219
	v_fmac_f32_e32 v245, v223, v223
	v_fmac_f32_e32 v244, v220, v220
	v_fmac_f32_e32 v245, v224, v224
	v_fmac_f32_e32 v244, v221, v221
	v_fmac_f32_e32 v245, v225, v225
	v_cvt_pk_fp8_f32 v240, v212, v213 op_sel:[0,0,1]
	v_cvt_pk_fp8_f32 v241, v216, v217 op_sel:[0,0,1]
	v_cvt_pk_fp8_f32 v242, v220, v221 op_sel:[0,0,1]
	v_cvt_pk_fp8_f32 v243, v224, v225 op_sel:[0,0,1]
	v_add_f32_e32 v244, v244, v245
	s_nop 0
	ds_write_b128 v228, v[240:243] offset:8704
	ds_write_b32 v229, v244 offset:40960
	global_load_dwordx4 v[194:197], v226, s[20:21] offset:0 nt
	global_load_dwordx4 v[198:201], v226, s[20:21] offset:128 nt
	global_load_dwordx4 v[202:205], v226, s[20:21] offset:256 nt
	global_load_dwordx4 v[206:209], v226, s[20:21] offset:384 nt
	s_waitcnt lgkmcnt(0)
	s_barrier
	ds_read_b128 v[162:165], v230 offset:8704
	ds_read_b128 v[166:169], v230 offset:8720
	ds_read_b128 v[170:173], v230 offset:8768
	ds_read_b128 v[174:177], v230 offset:8784
	ds_read_b128 v[178:181], v230 offset:8832
	ds_read_b128 v[182:185], v230 offset:8848
	ds_read_b128 v[186:189], v230 offset:8896
	ds_read_b128 v[190:193], v230 offset:8912
	s_waitcnt lgkmcnt(6)
	v_mfma_f32_32x32x64_f8f6f4 v[2:17], v[34:41], v[162:169], v[2:17]
	s_waitcnt lgkmcnt(4)
	v_mfma_f32_32x32x64_f8f6f4 v[2:17], v[26:33], v[170:177], v[2:17]
	v_min3_f32 v146, v146, v147, v148
	v_min3_f32 v149, v149, v150, v151
	v_min3_f32 v152, v152, v153, v154
	v_min3_f32 v155, v155, v156, v157
	v_min3_f32 v158, v158, v159, v160
	v_min3_f32 v146, v146, v149, v152
	v_min3_f32 v155, v155, v158, v161
	v_min3_f32 v235, v235, v146, v155
	ds_bpermute_b32 v246, v232, v235
	ds_read_b128 v[146:149], v231 offset:34944
	ds_read_b128 v[150:153], v231 offset:34976
	ds_read_b128 v[154:157], v231 offset:35008
	ds_read_b128 v[158:161], v231 offset:35040
	s_waitcnt lgkmcnt(7)
	v_mfma_f32_32x32x64_f8f6f4 v[2:17], v[50:57], v[178:185], v[2:17]
	s_waitcnt lgkmcnt(5)
	v_mfma_f32_32x32x64_f8f6f4 v[2:17], v[42:49], v[186:193], v[2:17]
	s_waitcnt lgkmcnt(0)
	v_min_f32_e32 v246, v235, v246
	ds_write_b32 v233, v246 offset:47104
	v_mfma_f32_32x32x64_f8f6f4 v[146:161], v[18:25], v[162:169], v[146:161]
	v_mfma_f32_32x32x64_f8f6f4 v[146:161], v[130:137], v[170:177], v[146:161]
	v_min3_f32 v2, v2, v3, v4
	v_min3_f32 v5, v5, v6, v7
	v_min3_f32 v8, v8, v9, v10
	v_min3_f32 v11, v11, v12, v13
	v_min3_f32 v14, v14, v15, v16
	v_min3_f32 v2, v2, v5, v8
	v_min3_f32 v11, v11, v14, v17
	v_min_f32_e32 v236, v2, v11
	ds_read_b128 v[2:5], v231 offset:35072
	ds_read_b128 v[6:9], v231 offset:35104
	ds_read_b128 v[10:13], v231 offset:35136
	ds_read_b128 v[14:17], v231 offset:35168
	v_mfma_f32_32x32x64_f8f6f4 v[146:161], v[122:129], v[178:185], v[146:161]
	v_mfma_f32_32x32x64_f8f6f4 v[146:161], v[138:145], v[186:193], v[146:161]
	s_waitcnt lgkmcnt(0)
	v_mfma_f32_32x32x64_f8f6f4 v[2:17], v[98:105], v[162:169], v[2:17]
	v_mfma_f32_32x32x64_f8f6f4 v[2:17], v[90:97], v[170:177], v[2:17]
	v_min3_f32 v146, v146, v147, v148
	v_min3_f32 v149, v149, v150, v151
	v_min3_f32 v152, v152, v153, v154
	v_min3_f32 v155, v155, v156, v157
	v_min3_f32 v158, v158, v159, v160
	v_min3_f32 v146, v146, v149, v152
	v_min3_f32 v155, v155, v158, v161
	v_min3_f32 v236, v236, v146, v155
	ds_read_b128 v[146:149], v231 offset:35200
	ds_read_b128 v[150:153], v231 offset:35232
	ds_read_b128 v[154:157], v231 offset:35264
	ds_read_b128 v[158:161], v231 offset:35296
	v_mfma_f32_32x32x64_f8f6f4 v[2:17], v[114:121], v[178:185], v[2:17]
	v_mfma_f32_32x32x64_f8f6f4 v[2:17], v[106:113], v[186:193], v[2:17]
	s_waitcnt lgkmcnt(0)
	v_mfma_f32_32x32x64_f8f6f4 v[146:161], v[58:65], v[162:169], v[146:161]
	v_mfma_f32_32x32x64_f8f6f4 v[146:161], v[66:73], v[170:177], v[146:161]
	v_min3_f32 v2, v2, v3, v4
	v_min3_f32 v5, v5, v6, v7
	v_min3_f32 v8, v8, v9, v10
	v_min3_f32 v11, v11, v12, v13
	v_min3_f32 v14, v14, v15, v16
	v_min3_f32 v2, v2, v5, v8
	v_min3_f32 v11, v11, v14, v17
	v_min3_f32 v236, v236, v2, v11
	ds_read_b128 v[2:5], v231 offset:34816
	ds_read_b128 v[6:9], v231 offset:34848
	ds_read_b128 v[10:13], v231 offset:34880
	ds_read_b128 v[14:17], v231 offset:34912
	v_mfma_f32_32x32x64_f8f6f4 v[146:161], v[74:81], v[178:185], v[146:161]
	v_mfma_f32_32x32x64_f8f6f4 v[146:161], v[82:89], v[186:193], v[146:161]
	s_waitcnt vmcnt(0)
	v_mul_f32_e32 v244, v194, v194
	v_mul_f32_e32 v245, v198, v198
	v_cvt_pk_fp8_f32 v240, v194, v195
	v_cvt_pk_fp8_f32 v241, v198, v199
	v_cvt_pk_fp8_f32 v242, v202, v203
	v_cvt_pk_fp8_f32 v243, v206, v207
	v_fmac_f32_e32 v244, v195, v195
	v_fmac_f32_e32 v245, v199, v199
	v_fmac_f32_e32 v244, v196, v196
	v_fmac_f32_e32 v245, v200, v200
	v_fmac_f32_e32 v244, v197, v197
	v_fmac_f32_e32 v245, v201, v201
	v_fmac_f32_e32 v244, v202, v202
	v_fmac_f32_e32 v245, v206, v206
	v_fmac_f32_e32 v244, v203, v203
	v_fmac_f32_e32 v245, v207, v207
	v_fmac_f32_e32 v244, v204, v204
	v_fmac_f32_e32 v245, v208, v208
	v_fmac_f32_e32 v244, v205, v205
	v_fmac_f32_e32 v245, v209, v209
	v_cvt_pk_fp8_f32 v240, v196, v197 op_sel:[0,0,1]
	v_cvt_pk_fp8_f32 v241, v200, v201 op_sel:[0,0,1]
	v_cvt_pk_fp8_f32 v242, v204, v205 op_sel:[0,0,1]
	v_cvt_pk_fp8_f32 v243, v208, v209 op_sel:[0,0,1]
	v_add_f32_e32 v244, v244, v245
	s_nop 0
	ds_write_b128 v228, v[240:243] offset:17408
	ds_write_b32 v229, v244 offset:43008
	global_load_dwordx4 v[210:213], v226, s[22:23] offset:0 nt
	global_load_dwordx4 v[214:217], v226, s[22:23] offset:128 nt
	global_load_dwordx4 v[218:221], v226, s[22:23] offset:256 nt
	global_load_dwordx4 v[222:225], v226, s[22:23] offset:384 nt
	s_waitcnt lgkmcnt(0)
	s_barrier
	ds_read_b128 v[162:165], v230 offset:17408
	ds_read_b128 v[166:169], v230 offset:17424
	ds_read_b128 v[170:173], v230 offset:17472
	ds_read_b128 v[174:177], v230 offset:17488
	ds_read_b128 v[178:181], v230 offset:17536
	ds_read_b128 v[182:185], v230 offset:17552
	ds_read_b128 v[186:189], v230 offset:17600
	ds_read_b128 v[190:193], v230 offset:17616
	s_waitcnt lgkmcnt(6)
	v_mfma_f32_32x32x64_f8f6f4 v[2:17], v[34:41], v[162:169], v[2:17]
	s_waitcnt lgkmcnt(4)
	v_mfma_f32_32x32x64_f8f6f4 v[2:17], v[26:33], v[170:177], v[2:17]
	v_min3_f32 v146, v146, v147, v148
	v_min3_f32 v149, v149, v150, v151
	v_min3_f32 v152, v152, v153, v154
	v_min3_f32 v155, v155, v156, v157
	v_min3_f32 v158, v158, v159, v160
	v_min3_f32 v146, v146, v149, v152
	v_min3_f32 v155, v155, v158, v161
	v_min3_f32 v236, v236, v146, v155
	ds_bpermute_b32 v246, v232, v236
	ds_read_b128 v[146:149], v231 offset:34944
	ds_read_b128 v[150:153], v231 offset:34976
	ds_read_b128 v[154:157], v231 offset:35008
	ds_read_b128 v[158:161], v231 offset:35040
	s_waitcnt lgkmcnt(7)
	v_mfma_f32_32x32x64_f8f6f4 v[2:17], v[50:57], v[178:185], v[2:17]
	s_waitcnt lgkmcnt(5)
	v_mfma_f32_32x32x64_f8f6f4 v[2:17], v[42:49], v[186:193], v[2:17]
	s_waitcnt lgkmcnt(0)
	v_min_f32_e32 v246, v236, v246
	ds_write_b32 v233, v246 offset:48128
	v_mfma_f32_32x32x64_f8f6f4 v[146:161], v[18:25], v[162:169], v[146:161]
	v_mfma_f32_32x32x64_f8f6f4 v[146:161], v[130:137], v[170:177], v[146:161]
	v_min3_f32 v2, v2, v3, v4
	v_min3_f32 v5, v5, v6, v7
	v_min3_f32 v8, v8, v9, v10
	v_min3_f32 v11, v11, v12, v13
	v_min3_f32 v14, v14, v15, v16
	v_min3_f32 v2, v2, v5, v8
	v_min3_f32 v11, v11, v14, v17
	v_min_f32_e32 v235, v2, v11
	ds_read_b128 v[2:5], v231 offset:35072
	ds_read_b128 v[6:9], v231 offset:35104
	ds_read_b128 v[10:13], v231 offset:35136
	ds_read_b128 v[14:17], v231 offset:35168
	v_mfma_f32_32x32x64_f8f6f4 v[146:161], v[122:129], v[178:185], v[146:161]
	v_mfma_f32_32x32x64_f8f6f4 v[146:161], v[138:145], v[186:193], v[146:161]
	s_waitcnt lgkmcnt(0)
	v_mfma_f32_32x32x64_f8f6f4 v[2:17], v[98:105], v[162:169], v[2:17]
	v_mfma_f32_32x32x64_f8f6f4 v[2:17], v[90:97], v[170:177], v[2:17]
	v_min3_f32 v146, v146, v147, v148
	v_min3_f32 v149, v149, v150, v151
	v_min3_f32 v152, v152, v153, v154
	v_min3_f32 v155, v155, v156, v157
	v_min3_f32 v158, v158, v159, v160
	v_min3_f32 v146, v146, v149, v152
	v_min3_f32 v155, v155, v158, v161
	v_min3_f32 v235, v235, v146, v155
	ds_read_b128 v[146:149], v231 offset:35200
	ds_read_b128 v[150:153], v231 offset:35232
	ds_read_b128 v[154:157], v231 offset:35264
	ds_read_b128 v[158:161], v231 offset:35296
	v_mfma_f32_32x32x64_f8f6f4 v[2:17], v[114:121], v[178:185], v[2:17]
	v_mfma_f32_32x32x64_f8f6f4 v[2:17], v[106:113], v[186:193], v[2:17]
	s_waitcnt lgkmcnt(0)
	v_mfma_f32_32x32x64_f8f6f4 v[146:161], v[58:65], v[162:169], v[146:161]
	v_mfma_f32_32x32x64_f8f6f4 v[146:161], v[66:73], v[170:177], v[146:161]
	v_min3_f32 v2, v2, v3, v4
	v_min3_f32 v5, v5, v6, v7
	v_min3_f32 v8, v8, v9, v10
	v_min3_f32 v11, v11, v12, v13
	v_min3_f32 v14, v14, v15, v16
	v_min3_f32 v2, v2, v5, v8
	v_min3_f32 v11, v11, v14, v17
	v_min3_f32 v235, v235, v2, v11
	ds_read_b128 v[2:5], v231 offset:34816
	ds_read_b128 v[6:9], v231 offset:34848
	ds_read_b128 v[10:13], v231 offset:34880
	ds_read_b128 v[14:17], v231 offset:34912
	v_mfma_f32_32x32x64_f8f6f4 v[146:161], v[74:81], v[178:185], v[146:161]
	v_mfma_f32_32x32x64_f8f6f4 v[146:161], v[82:89], v[186:193], v[146:161]
	s_waitcnt vmcnt(0)
	v_mul_f32_e32 v244, v210, v210
	v_mul_f32_e32 v245, v214, v214
	v_cvt_pk_fp8_f32 v240, v210, v211
	v_cvt_pk_fp8_f32 v241, v214, v215
	v_cvt_pk_fp8_f32 v242, v218, v219
	v_cvt_pk_fp8_f32 v243, v222, v223
	v_fmac_f32_e32 v244, v211, v211
	v_fmac_f32_e32 v245, v215, v215
	v_fmac_f32_e32 v244, v212, v212
	v_fmac_f32_e32 v245, v216, v216
	v_fmac_f32_e32 v244, v213, v213
	v_fmac_f32_e32 v245, v217, v217
	v_fmac_f32_e32 v244, v218, v218
	v_fmac_f32_e32 v245, v222, v222
	v_fmac_f32_e32 v244, v219, v219
	v_fmac_f32_e32 v245, v223, v223
	v_fmac_f32_e32 v244, v220, v220
	v_fmac_f32_e32 v245, v224, v224
	v_fmac_f32_e32 v244, v221, v221
	v_fmac_f32_e32 v245, v225, v225
	v_cvt_pk_fp8_f32 v240, v212, v213 op_sel:[0,0,1]
	v_cvt_pk_fp8_f32 v241, v216, v217 op_sel:[0,0,1]
	v_cvt_pk_fp8_f32 v242, v220, v221 op_sel:[0,0,1]
	v_cvt_pk_fp8_f32 v243, v224, v225 op_sel:[0,0,1]
	v_add_f32_e32 v244, v244, v245
	s_nop 0
	ds_write_b128 v228, v[240:243] offset:26112
	ds_write_b32 v229, v244 offset:45056
	s_waitcnt lgkmcnt(0)
	s_barrier
	ds_read_b128 v[162:165], v230 offset:26112
	ds_read_b128 v[166:169], v230 offset:26128
	ds_read_b128 v[170:173], v230 offset:26176
	ds_read_b128 v[174:177], v230 offset:26192
	ds_read_b128 v[178:181], v230 offset:26240
	ds_read_b128 v[182:185], v230 offset:26256
	ds_read_b128 v[186:189], v230 offset:26304
	ds_read_b128 v[190:193], v230 offset:26320
	s_waitcnt lgkmcnt(6)
	v_mfma_f32_32x32x64_f8f6f4 v[2:17], v[34:41], v[162:169], v[2:17]
	s_waitcnt lgkmcnt(4)
	v_mfma_f32_32x32x64_f8f6f4 v[2:17], v[26:33], v[170:177], v[2:17]
	v_min3_f32 v146, v146, v147, v148
	v_min3_f32 v149, v149, v150, v151
	v_min3_f32 v152, v152, v153, v154
	v_min3_f32 v155, v155, v156, v157
	v_min3_f32 v158, v158, v159, v160
	v_min3_f32 v146, v146, v149, v152
	v_min3_f32 v155, v155, v158, v161
	v_min3_f32 v235, v235, v146, v155
	ds_bpermute_b32 v246, v232, v235
	ds_read_b128 v[146:149], v231 offset:34944
	ds_read_b128 v[150:153], v231 offset:34976
	ds_read_b128 v[154:157], v231 offset:35008
	ds_read_b128 v[158:161], v231 offset:35040
	s_waitcnt lgkmcnt(7)
	v_mfma_f32_32x32x64_f8f6f4 v[2:17], v[50:57], v[178:185], v[2:17]
	s_waitcnt lgkmcnt(5)
	v_mfma_f32_32x32x64_f8f6f4 v[2:17], v[42:49], v[186:193], v[2:17]
	s_waitcnt lgkmcnt(0)
	v_min_f32_e32 v246, v235, v246
	ds_write_b32 v233, v246 offset:49152
	v_mfma_f32_32x32x64_f8f6f4 v[146:161], v[18:25], v[162:169], v[146:161]
	v_mfma_f32_32x32x64_f8f6f4 v[146:161], v[130:137], v[170:177], v[146:161]
	v_min3_f32 v2, v2, v3, v4
	v_min3_f32 v5, v5, v6, v7
	v_min3_f32 v8, v8, v9, v10
	v_min3_f32 v11, v11, v12, v13
	v_min3_f32 v14, v14, v15, v16
	v_min3_f32 v2, v2, v5, v8
	v_min3_f32 v11, v11, v14, v17
	v_min_f32_e32 v236, v2, v11
	ds_read_b128 v[2:5], v231 offset:35072
	ds_read_b128 v[6:9], v231 offset:35104
	ds_read_b128 v[10:13], v231 offset:35136
	ds_read_b128 v[14:17], v231 offset:35168
	v_mfma_f32_32x32x64_f8f6f4 v[146:161], v[122:129], v[178:185], v[146:161]
	v_mfma_f32_32x32x64_f8f6f4 v[146:161], v[138:145], v[186:193], v[146:161]
	s_waitcnt lgkmcnt(0)
	v_mfma_f32_32x32x64_f8f6f4 v[2:17], v[98:105], v[162:169], v[2:17]
	v_mfma_f32_32x32x64_f8f6f4 v[2:17], v[90:97], v[170:177], v[2:17]
	v_min3_f32 v146, v146, v147, v148
	v_min3_f32 v149, v149, v150, v151
	v_min3_f32 v152, v152, v153, v154
	v_min3_f32 v155, v155, v156, v157
	v_min3_f32 v158, v158, v159, v160
	v_min3_f32 v146, v146, v149, v152
	v_min3_f32 v155, v155, v158, v161
	v_min3_f32 v236, v236, v146, v155
	ds_read_b128 v[146:149], v231 offset:35200
	ds_read_b128 v[150:153], v231 offset:35232
	ds_read_b128 v[154:157], v231 offset:35264
	ds_read_b128 v[158:161], v231 offset:35296
	v_mfma_f32_32x32x64_f8f6f4 v[2:17], v[114:121], v[178:185], v[2:17]
	v_mfma_f32_32x32x64_f8f6f4 v[2:17], v[106:113], v[186:193], v[2:17]
	s_waitcnt lgkmcnt(0)
	v_mfma_f32_32x32x64_f8f6f4 v[146:161], v[58:65], v[162:169], v[146:161]
	v_mfma_f32_32x32x64_f8f6f4 v[146:161], v[66:73], v[170:177], v[146:161]
	v_min3_f32 v2, v2, v3, v4
	v_min3_f32 v5, v5, v6, v7
	v_min3_f32 v8, v8, v9, v10
	v_min3_f32 v11, v11, v12, v13
	v_min3_f32 v14, v14, v15, v16
	v_min3_f32 v2, v2, v5, v8
	v_min3_f32 v11, v11, v14, v17
	v_min3_f32 v236, v236, v2, v11
	v_mfma_f32_32x32x64_f8f6f4 v[146:161], v[74:81], v[178:185], v[146:161]
	v_mfma_f32_32x32x64_f8f6f4 v[146:161], v[82:89], v[186:193], v[146:161]
	v_cmp_gt_u32_e32 vcc, 0x80, v0
	s_and_saveexec_b64 s[34:35], vcc
	v_lshlrev_b32_e32 v36, 6, v0
	ds_read_b128 v[20:23], v36 offset:38912
	ds_read_b128 v[24:27], v36 offset:38928
	ds_read_b128 v[28:31], v36 offset:38944
	ds_read_b128 v[32:35], v36 offset:38960
	s_mov_b64 exec, s[34:35]
	s_nop 15
	s_nop 3
	v_min3_f32 v146, v146, v147, v148
	v_min3_f32 v149, v149, v150, v151
	v_min3_f32 v152, v152, v153, v154
	v_min3_f32 v155, v155, v156, v157
	v_min3_f32 v158, v158, v159, v160
	v_min3_f32 v146, v146, v149, v152
	v_min3_f32 v155, v155, v158, v161
	v_min3_f32 v236, v236, v146, v155
	ds_bpermute_b32 v246, v232, v236
	s_waitcnt lgkmcnt(0)
	v_min_f32_e32 v246, v236, v246
	ds_write_b32 v233, v246 offset:50176
	s_waitcnt lgkmcnt(0)
	s_barrier
	v_readfirstlane_b32 s2, v1
	s_nop 3
	s_cmp_gt_u32 s2, 1
	s_cbranch_scc1 .Lmain_end
	v_and_b32_e32 v2, 31, v0
	v_lshlrev_b32_e32 v3, 5, v0
	v_and_b32_e32 v3, 0xc00, v3
	v_lshl_or_b32 v8, v2, 2, v3
	v_add_u32_e32 v8, 0xb800, v8
	ds_read2_b32 v[2:3], v8 offset1:32
	ds_read2_b32 v[4:5], v8 offset0:64 offset1:96
	ds_read2_b32 v[6:7], v8 offset0:128 offset1:160
	ds_read2_b32 v[10:11], v8 offset0:192 offset1:224
	s_mov_b32 s8, 0xf800000
	s_lshr_b32 s2, s30, 3
	s_lshl_b32 s2, s2, 7
	s_add_u32 s2, s2, 0x300000
	s_add_u32 s6, s6, s2
	s_addc_u32 s7, s7, 0
	s_mov_b32 s4, 0
	s_mov_b32 s5, 0x41d00000
	s_mov_b32 s16, 0
	s_mov_b32 s17, 0x420e0000
	s_waitcnt lgkmcnt(0)
	v_min3_f32 v2, v2, v3, v4
	v_min3_f32 v5, v5, v6, v7
	v_min3_f32 v2, v2, v10, v11
	v_min_f32_e32 v2, v2, v5
	s_waitcnt lgkmcnt(0)
	v_add_f32_e32 v20, v20, v21
	v_add_f32_e32 v22, v22, v23
	v_add_f32_e32 v24, v24, v25
	v_add_f32_e32 v26, v26, v27
	v_add_f32_e32 v28, v28, v29
	v_add_f32_e32 v30, v30, v31
	v_add_f32_e32 v32, v32, v33
	v_add_f32_e32 v34, v34, v35
	v_add_f32_e32 v20, v20, v22
	v_add_f32_e32 v24, v24, v26
	v_add_f32_e32 v28, v28, v30
	v_add_f32_e32 v32, v32, v34
	v_add_f32_e32 v20, v20, v24
	v_add_f32_e32 v28, v28, v32
	v_add_f32_e32 v20, v20, v28
	v_add_f32_e32 v2, v2, v20
	v_max_f32_e32 v2, 0, v2
	v_mul_f32_e32 v3, 0x4f800000, v2
	v_cmp_gt_f32_e32 vcc, s8, v2
	s_nop 1
	v_cndmask_b32_e32 v2, v2, v3, vcc
	v_sqrt_f32_e32 v3, v2
	s_nop 0
	v_add_u32_e32 v4, -1, v3
	v_fma_f32 v5, -v4, v3, v2
	v_cmp_ge_f32_e64 s[18:19], 0, v5
	v_add_u32_e32 v5, 1, v3
	s_nop 0
	v_cndmask_b32_e64 v4, v3, v4, s[18:19]
	v_fma_f32 v3, -v5, v3, v2
	v_cmp_lt_f32_e64 s[18:19], 0, v3
	s_nop 1
	v_cndmask_b32_e64 v3, v4, v5, s[18:19]
	v_mul_f32_e32 v4, 0x37800000, v3
	v_cndmask_b32_e32 v3, v3, v4, vcc
	v_mov_b32_e32 v4, 0x260
	v_cmp_class_f32_e32 vcc, v2, v4
	s_nop 1
	v_cndmask_b32_e32 v2, v3, v2, vcc
	s_nop 1
	v_add_f32_dpp v3, v2, v2 quad_perm:[1,0,3,2] row_mask:0xf bank_mask:0xf
	s_nop 1
	v_add_f32_dpp v4, v3, v3 quad_perm:[2,3,0,1] row_mask:0xf bank_mask:0xf
	s_nop 1
	v_add_f32_dpp v5, v4, v4 row_half_mirror row_mask:0xf bank_mask:0xf
	s_nop 1
	v_add_f32_dpp v6, v5, v5 row_mirror row_mask:0xf bank_mask:0xf
	s_nop 1
	v_readlane_b32 s12, v6, 0
	v_readlane_b32 s13, v6, 16
	v_readlane_b32 s14, v6, 32
	v_readlane_b32 s15, v6, 48
	s_nop 3
	v_mov_b32_e32 v7, s12
	v_add_f32_e32 v7, s13, v7
	v_mov_b32_e32 v9, s14
	v_add_f32_e32 v9, s15, v9
	v_add_f32_e32 v0, v7, v9
	v_mov_b32_e32 v4, 0
	s_mov_b64 exec, 1
	v_cvt_f64_f32_e32 v[6:7], v0
	v_add_f64 v[8:9], v[6:7], s[4:5]
	global_atomic_add_f64 v[10:11], v4, v[8:9], s[6:7] sc0
	s_waitcnt vmcnt(0)
	v_cmp_le_f64_e32 vcc, s[16:17], v[10:11]
	s_and_saveexec_b64 s[2:3], vcc
	s_cbranch_execz .Lmain_end
	v_add_f64 v[10:11], v[10:11], -s[16:17]
	v_add_f64 v[10:11], v[10:11], v[6:7]
	v_cvt_f32_f64_e32 v0, v[10:11]
	v_mul_f32_e32 v0, 0x38000000, v0
	global_atomic_add_f32 v4, v0, s[10:11]
